# expert-choice slot table stored sample-expert-token (top-k writes 16 consecutive tokens per thread into one line instead of 16 lines shared with other XCDs); final phase gathers the 32 words of a toke
# baseline (speedup 1.0000x reference)
.Lxb_poll_0:
.Lxb_spin_0:
	global_load_dword v238, v237, s[100:101] sc1
	s_waitcnt vmcnt(0)
	v_cmp_ge_u32_e32 vcc, v238, v236
	s_cbranch_vccnz .Lxb_done_0
	s_sleep 1
	v_add_u32_e32 v239, 1, v239
	v_cmp_gt_u32_e32 vcc, 0x200000, v239
	s_cbranch_vccnz .Lxb_spin_0

.LBB0_727:
	s_or_b64 exec, exec, s[0:1]
	v_add_u32_e32 v2, s28, v62
	v_readlane_b32 s0, v235, 0
	v_ashrrev_i32_e32 v3, 31, v2
	v_readlane_b32 s2, v235, 2
	v_lshlrev_b64 v[2:3], 2, v[2:3]
	s_add_i32 s43, s43, s2
	s_add_i32 s33, s33, s47
	v_lshl_add_u64 v[2:3], s[26:27], 0, v[2:3]
	s_cmp_gt_i32 s43, 31
	v_lshl_add_u64 v[30:31], v[30:31], 0, s[38:39]
	global_store_dword v[2:3], v0, off
	v_readlane_b32 s1, v235, 1
	v_readlane_b32 s3, v235, 3
	s_cbranch_scc1 .LBB0_918

.LBB0_888:
	s_or_b64 exec, exec, vcc
	v_cndmask_b32_e64 v12, 0, 1, s[26:27]
	v_cndmask_b32_e64 v75, 0, 1, s[28:29]
	s_lshl_b32 s28, s46, 13
	s_mul_i32 s26, s46, 15
	s_add_i32 s26, s26, s45
	s_lshl_b32 s26, s26, 15
	v_readlane_b32 s27, v235, 20
	v_add_u32_e32 v76, s28, v20
	v_add_u32_sdwa v12, v73, v12 dst_sel:DWORD dst_unused:UNUSED_PAD src0_sel:WORD_0 src1_sel:DWORD
	v_add_u32_sdwa v73, sext(v73), v75 dst_sel:DWORD dst_unused:UNUSED_PAD src0_sel:WORD_1 src1_sel:DWORD
	s_add_u32 s26, s27, s26
	v_readlane_b32 s27, v235, 21
	v_ashrrev_i32_e32 v77, 31, v76
	v_cmp_lt_i32_e32 vcc, v73, v17
	s_addc_u32 s27, s27, 0
	v_lshlrev_b64 v[76:77], 2, v[76:77]
	s_and_b64 s[24:25], s[24:25], vcc
	v_lshl_add_u64 v[76:77], s[26:27], 0, v[76:77]
	s_or_b64 s[24:25], s[2:3], s[24:25]
	global_store_dword v[76:77], v74, off
	s_and_saveexec_b64 s[2:3], s[24:25]
	s_cbranch_execz .LBB0_890
	v_min_i32_e32 v72, v73, v17
	v_add_u32_e32 v72, v72, v12
	v_add_u32_e32 v74, s33, v72
	v_ashrrev_i32_e32 v75, 31, v74
	v_lshlrev_b64 v[74:75], 2, v[74:75]
	v_lshl_add_u64 v[76:77], s[30:31], 0, v[74:75]
	v_lshl_add_u64 v[74:75], s[34:35], 0, v[74:75]
	global_store_dword v[74:75], v13, off
	v_add_u32_e32 v74, s44, v72
	v_ashrrev_i32_e32 v75, 31, v74
	v_lshl_add_u64 v[74:75], v[74:75], 2, s[36:37]
	global_store_dword v[76:77], v48, off
	global_store_dword v[74:75], v13, off
.LBB0_890:
	s_or_b64 exec, exec, s[2:3]
	v_add_u32_e32 v74, s28, v48
	v_add_u32_e32 v13, v12, v70
	v_add_u32_e32 v70, v73, v71
	v_ashrrev_i32_e32 v75, 31, v74
	v_cmp_lt_i32_e32 vcc, v70, v17
	v_lshlrev_b64 v[74:75], 2, v[74:75]
	s_and_b64 s[0:1], s[0:1], vcc
	v_lshl_add_u64 v[74:75], s[26:27], 0, v[74:75]
	s_or_b64 s[2:3], s[20:21], s[0:1]
	v_mov_b32_e32 v12, -1
	v_mov_b32_e32 v71, -1
	global_store_dword v[74:75], v72, off
	s_and_saveexec_b64 s[0:1], s[2:3]
	s_cbranch_execz .LBB0_892
	v_min_i32_e32 v71, v70, v17
	v_add_u32_e32 v71, v71, v13
	v_add_u32_e32 v72, s33, v71
	v_ashrrev_i32_e32 v73, 31, v72
	v_lshlrev_b64 v[72:73], 2, v[72:73]
	v_lshl_add_u64 v[74:75], s[30:31], 0, v[72:73]
	v_lshl_add_u64 v[72:73], s[34:35], 0, v[72:73]
	global_store_dword v[72:73], v14, off
	v_add_u32_e32 v72, s44, v71
	v_ashrrev_i32_e32 v73, 31, v72
	v_lshl_add_u64 v[72:73], v[72:73], 2, s[36:37]
	global_store_dword v[74:75], v49, off
	global_store_dword v[72:73], v14, off
.LBB0_892:
	s_or_b64 exec, exec, s[0:1]
	v_add_u32_e32 v72, s28, v49
	v_add_u32_e32 v14, v70, v69
	v_ashrrev_i32_e32 v73, 31, v72
	v_cmp_lt_i32_e32 vcc, v14, v17
	v_lshlrev_b64 v[72:73], 2, v[72:73]
	s_and_b64 s[0:1], s[22:23], vcc
	v_lshl_add_u64 v[72:73], s[26:27], 0, v[72:73]
	v_add_u32_e32 v13, v13, v68
	s_or_b64 s[2:3], s[96:97], s[0:1]
	global_store_dword v[72:73], v71, off
	s_and_saveexec_b64 s[0:1], s[2:3]
	s_cbranch_execz .LBB0_894
	v_min_i32_e32 v12, v14, v17
	v_add_u32_e32 v12, v12, v13
	v_add_u32_e32 v68, s33, v12
	v_ashrrev_i32_e32 v69, 31, v68
	v_lshlrev_b64 v[68:69], 2, v[68:69]
	v_lshl_add_u64 v[70:71], s[30:31], 0, v[68:69]
	v_lshl_add_u64 v[68:69], s[34:35], 0, v[68:69]
	global_store_dword v[68:69], v15, off
	v_add_u32_e32 v68, s44, v12
	v_ashrrev_i32_e32 v69, 31, v68
	v_lshl_add_u64 v[68:69], v[68:69], 2, s[36:37]
	global_store_dword v[70:71], v50, off
	global_store_dword v[68:69], v15, off
.LBB0_894:
	s_or_b64 exec, exec, s[0:1]
	v_cndmask_b32_e64 v70, 0, 1, s[22:23]
	v_add_u32_e32 v68, s28, v50
	v_ashrrev_i32_e32 v69, 31, v68
	v_add_u32_e32 v14, v14, v70
	v_lshlrev_b64 v[68:69], 2, v[68:69]
	v_cmp_lt_i32_e32 vcc, v14, v17
	v_cndmask_b32_e64 v15, 0, 1, s[96:97]
	v_lshl_add_u64 v[68:69], s[26:27], 0, v[68:69]
	s_and_b64 s[0:1], s[94:95], vcc
	global_store_dword v[68:69], v12, off
	v_add_u32_e32 v13, v13, v15
	s_or_b64 s[2:3], s[92:93], s[0:1]
	v_mov_b32_e32 v12, -1
	v_mov_b32_e32 v15, -1
	s_and_saveexec_b64 s[0:1], s[2:3]
	s_cbranch_execz .LBB0_896
	v_min_i32_e32 v15, v14, v17
	v_add_u32_e32 v15, v15, v13
	v_add_u32_e32 v68, s33, v15
	v_ashrrev_i32_e32 v69, 31, v68
	v_lshlrev_b64 v[68:69], 2, v[68:69]
	v_lshl_add_u64 v[70:71], s[30:31], 0, v[68:69]
	v_lshl_add_u64 v[68:69], s[34:35], 0, v[68:69]
	global_store_dword v[68:69], v8, off
	v_add_u32_e32 v68, s44, v15
	v_ashrrev_i32_e32 v69, 31, v68
	v_lshl_add_u64 v[68:69], v[68:69], 2, s[36:37]
	global_store_dword v[70:71], v51, off
	global_store_dword v[68:69], v8, off
.LBB0_896:
	s_or_b64 exec, exec, s[0:1]
	v_add_u32_e32 v68, s28, v51
	v_add_u32_e32 v8, v13, v66
	v_add_u32_e32 v13, v14, v67
	v_ashrrev_i32_e32 v69, 31, v68
	v_cmp_lt_i32_e32 vcc, v13, v17
	v_lshlrev_b64 v[68:69], 2, v[68:69]
	s_and_b64 s[0:1], s[90:91], vcc
	v_lshl_add_u64 v[68:69], s[26:27], 0, v[68:69]
	s_or_b64 s[2:3], s[88:89], s[0:1]
	global_store_dword v[68:69], v15, off
	s_and_saveexec_b64 s[0:1], s[2:3]
	s_cbranch_execz .LBB0_898
	v_min_i32_e32 v12, v13, v17
	v_add_u32_e32 v12, v12, v8
	v_add_u32_e32 v14, s33, v12
	v_ashrrev_i32_e32 v15, 31, v14
	v_lshlrev_b64 v[14:15], 2, v[14:15]
	v_lshl_add_u64 v[66:67], s[30:31], 0, v[14:15]
	v_lshl_add_u64 v[14:15], s[34:35], 0, v[14:15]
	global_store_dword v[14:15], v9, off
	v_add_u32_e32 v14, s44, v12
	v_ashrrev_i32_e32 v15, 31, v14
	v_lshl_add_u64 v[14:15], v[14:15], 2, s[36:37]
	global_store_dword v[66:67], v52, off
	global_store_dword v[14:15], v9, off
.LBB0_898:
	s_or_b64 exec, exec, s[0:1]
	v_add_u32_e32 v14, s28, v52
	v_ashrrev_i32_e32 v15, 31, v14
	v_lshlrev_b64 v[14:15], 2, v[14:15]
	v_cndmask_b32_e64 v66, 0, 1, s[90:91]
	v_lshl_add_u64 v[14:15], s[26:27], 0, v[14:15]
	global_store_dword v[14:15], v12, off
	v_add_u32_e32 v12, v13, v66
	v_cmp_lt_i32_e32 vcc, v12, v17
	v_cndmask_b32_e64 v9, 0, 1, s[88:89]
	s_and_b64 s[0:1], s[86:87], vcc
	v_add_u32_e32 v9, v8, v9
	s_or_b64 s[2:3], s[84:85], s[0:1]
	v_mov_b32_e32 v8, -1
	v_mov_b32_e32 v13, -1
	s_and_saveexec_b64 s[0:1], s[2:3]
	s_cbranch_execz .LBB0_900
	v_min_i32_e32 v13, v12, v17
	v_add_u32_e32 v13, v13, v9
	v_add_u32_e32 v14, s33, v13
	v_ashrrev_i32_e32 v15, 31, v14
	v_lshlrev_b64 v[14:15], 2, v[14:15]
	v_lshl_add_u64 v[66:67], s[30:31], 0, v[14:15]
	v_lshl_add_u64 v[14:15], s[34:35], 0, v[14:15]
	global_store_dword v[14:15], v10, off
	v_add_u32_e32 v14, s44, v13
	v_ashrrev_i32_e32 v15, 31, v14
	v_lshl_add_u64 v[14:15], v[14:15], 2, s[36:37]
	global_store_dword v[66:67], v53, off
	global_store_dword v[14:15], v10, off
.LBB0_900:
	s_or_b64 exec, exec, s[0:1]
	v_add_u32_e32 v14, s28, v53
	v_add_u32_e32 v10, v12, v65
	v_ashrrev_i32_e32 v15, 31, v14
	v_cmp_lt_i32_e32 vcc, v10, v17
	v_lshlrev_b64 v[14:15], 2, v[14:15]
	s_and_b64 s[0:1], s[82:83], vcc
	v_lshl_add_u64 v[14:15], s[26:27], 0, v[14:15]
	v_add_u32_e32 v9, v9, v33
	s_or_b64 s[2:3], s[80:81], s[0:1]
	global_store_dword v[14:15], v13, off
	s_and_saveexec_b64 s[0:1], s[2:3]
	s_cbranch_execz .LBB0_902
	v_min_i32_e32 v8, v10, v17
	v_add_u32_e32 v8, v8, v9
	v_add_u32_e32 v12, s33, v8
	v_ashrrev_i32_e32 v13, 31, v12
	v_lshlrev_b64 v[12:13], 2, v[12:13]
	v_lshl_add_u64 v[14:15], s[30:31], 0, v[12:13]
	v_lshl_add_u64 v[12:13], s[34:35], 0, v[12:13]
	global_store_dword v[12:13], v11, off
	v_add_u32_e32 v12, s44, v8
	v_ashrrev_i32_e32 v13, 31, v12
	v_lshl_add_u64 v[12:13], v[12:13], 2, s[36:37]
	global_store_dword v[14:15], v54, off
	global_store_dword v[12:13], v11, off
.LBB0_902:
	s_or_b64 exec, exec, s[0:1]
	v_cndmask_b32_e64 v14, 0, 1, s[82:83]
	v_add_u32_e32 v12, s28, v54
	v_ashrrev_i32_e32 v13, 31, v12
	v_add_u32_e32 v10, v10, v14
	v_lshlrev_b64 v[12:13], 2, v[12:13]
	v_cmp_lt_i32_e32 vcc, v10, v17
	v_cndmask_b32_e64 v11, 0, 1, s[80:81]
	v_lshl_add_u64 v[12:13], s[26:27], 0, v[12:13]
	s_and_b64 s[0:1], s[78:79], vcc
	global_store_dword v[12:13], v8, off
	v_add_u32_e32 v9, v9, v11
	s_or_b64 s[2:3], s[76:77], s[0:1]
	v_mov_b32_e32 v8, -1
	v_mov_b32_e32 v11, -1
	s_and_saveexec_b64 s[0:1], s[2:3]
	s_cbranch_execz .LBB0_904
	v_min_i32_e32 v11, v10, v17
	v_add_u32_e32 v11, v11, v9
	v_add_u32_e32 v12, s33, v11
	v_ashrrev_i32_e32 v13, 31, v12
	v_lshlrev_b64 v[12:13], 2, v[12:13]
	v_lshl_add_u64 v[14:15], s[30:31], 0, v[12:13]
	v_lshl_add_u64 v[12:13], s[34:35], 0, v[12:13]
	global_store_dword v[12:13], v4, off
	v_add_u32_e32 v12, s44, v11
	v_ashrrev_i32_e32 v13, 31, v12
	v_lshl_add_u64 v[12:13], v[12:13], 2, s[36:37]
	global_store_dword v[14:15], v55, off
	global_store_dword v[12:13], v4, off
.LBB0_904:
	s_or_b64 exec, exec, s[0:1]
	v_add_u32_e32 v12, s28, v55
	v_add_u32_e32 v4, v9, v29
	v_add_u32_e32 v9, v10, v32
	v_ashrrev_i32_e32 v13, 31, v12
	v_cmp_lt_i32_e32 vcc, v9, v17
	v_lshlrev_b64 v[12:13], 2, v[12:13]
	s_and_b64 s[0:1], s[74:75], vcc
	v_lshl_add_u64 v[12:13], s[26:27], 0, v[12:13]
	s_or_b64 s[2:3], s[72:73], s[0:1]
	global_store_dword v[12:13], v11, off
	s_and_saveexec_b64 s[0:1], s[2:3]
	s_cbranch_execz .LBB0_906
	v_min_i32_e32 v8, v9, v17
	v_add_u32_e32 v8, v8, v4
	v_add_u32_e32 v10, s33, v8
	v_ashrrev_i32_e32 v11, 31, v10
	v_lshlrev_b64 v[10:11], 2, v[10:11]
	v_lshl_add_u64 v[12:13], s[30:31], 0, v[10:11]
	v_lshl_add_u64 v[10:11], s[34:35], 0, v[10:11]
	global_store_dword v[10:11], v5, off
	v_add_u32_e32 v10, s44, v8
	v_ashrrev_i32_e32 v11, 31, v10
	v_lshl_add_u64 v[10:11], v[10:11], 2, s[36:37]
	global_store_dword v[12:13], v56, off
	global_store_dword v[10:11], v5, off
.LBB0_906:
	s_or_b64 exec, exec, s[0:1]
	v_add_u32_e32 v10, s28, v56
	v_ashrrev_i32_e32 v11, 31, v10
	v_lshlrev_b64 v[10:11], 2, v[10:11]
	v_cndmask_b32_e64 v12, 0, 1, s[74:75]
	v_lshl_add_u64 v[10:11], s[26:27], 0, v[10:11]
	global_store_dword v[10:11], v8, off
	v_add_u32_e32 v8, v9, v12
	v_cmp_lt_i32_e32 vcc, v8, v17
	v_cndmask_b32_e64 v5, 0, 1, s[72:73]
	s_and_b64 s[0:1], s[70:71], vcc
	v_add_u32_e32 v5, v4, v5
	s_or_b64 s[2:3], s[68:69], s[0:1]
	v_mov_b32_e32 v4, -1
	v_mov_b32_e32 v9, -1
	s_and_saveexec_b64 s[0:1], s[2:3]
	s_cbranch_execz .LBB0_908
	v_min_i32_e32 v9, v8, v17
	v_add_u32_e32 v9, v9, v5
	v_add_u32_e32 v10, s33, v9
	v_ashrrev_i32_e32 v11, 31, v10
	v_lshlrev_b64 v[10:11], 2, v[10:11]
	v_lshl_add_u64 v[12:13], s[30:31], 0, v[10:11]
	v_lshl_add_u64 v[10:11], s[34:35], 0, v[10:11]
	global_store_dword v[10:11], v6, off
	v_add_u32_e32 v10, s44, v9
	v_ashrrev_i32_e32 v11, 31, v10
	v_lshl_add_u64 v[10:11], v[10:11], 2, s[36:37]
	global_store_dword v[12:13], v57, off
	global_store_dword v[10:11], v6, off
.LBB0_908:
	s_or_b64 exec, exec, s[0:1]
	v_add_u32_e32 v10, s28, v57
	v_add_u32_e32 v6, v8, v27
	v_ashrrev_i32_e32 v11, 31, v10
	v_cmp_lt_i32_e32 vcc, v6, v17
	v_lshlrev_b64 v[10:11], 2, v[10:11]
	s_and_b64 s[0:1], s[66:67], vcc
	v_lshl_add_u64 v[10:11], s[26:27], 0, v[10:11]
	v_add_u32_e32 v5, v5, v25
	s_or_b64 s[2:3], s[64:65], s[0:1]
	global_store_dword v[10:11], v9, off
	s_and_saveexec_b64 s[0:1], s[2:3]
	s_cbranch_execz .LBB0_910
	v_min_i32_e32 v4, v6, v17
	v_add_u32_e32 v4, v4, v5
	v_add_u32_e32 v8, s33, v4
	v_ashrrev_i32_e32 v9, 31, v8
	v_lshlrev_b64 v[8:9], 2, v[8:9]
	v_lshl_add_u64 v[10:11], s[30:31], 0, v[8:9]
	v_lshl_add_u64 v[8:9], s[34:35], 0, v[8:9]
	global_store_dword v[8:9], v7, off
	v_add_u32_e32 v8, s44, v4
	v_ashrrev_i32_e32 v9, 31, v8
	v_lshl_add_u64 v[8:9], v[8:9], 2, s[36:37]
	global_store_dword v[10:11], v58, off
	global_store_dword v[8:9], v7, off
.LBB0_910:
	s_or_b64 exec, exec, s[0:1]
	v_cndmask_b32_e64 v10, 0, 1, s[66:67]
	v_add_u32_e32 v8, s28, v58
	v_ashrrev_i32_e32 v9, 31, v8
	v_add_u32_e32 v6, v6, v10
	v_lshlrev_b64 v[8:9], 2, v[8:9]
	v_cmp_lt_i32_e32 vcc, v6, v17
	v_cndmask_b32_e64 v7, 0, 1, s[64:65]
	v_lshl_add_u64 v[8:9], s[26:27], 0, v[8:9]
	s_and_b64 s[0:1], s[62:63], vcc
	global_store_dword v[8:9], v4, off
	v_add_u32_e32 v5, v5, v7
	s_or_b64 s[2:3], s[60:61], s[0:1]
	v_mov_b32_e32 v4, -1
	v_mov_b32_e32 v7, -1
	s_and_saveexec_b64 s[0:1], s[2:3]
	s_cbranch_execz .LBB0_912
	v_min_i32_e32 v7, v6, v17
	v_add_u32_e32 v7, v7, v5
	v_add_u32_e32 v8, s33, v7
	v_ashrrev_i32_e32 v9, 31, v8
	v_lshlrev_b64 v[8:9], 2, v[8:9]
	v_lshl_add_u64 v[10:11], s[30:31], 0, v[8:9]
	v_lshl_add_u64 v[8:9], s[34:35], 0, v[8:9]
	global_store_dword v[8:9], v0, off
	v_add_u32_e32 v8, s44, v7
	v_ashrrev_i32_e32 v9, 31, v8
	v_lshl_add_u64 v[8:9], v[8:9], 2, s[36:37]
	global_store_dword v[10:11], v59, off
	global_store_dword v[8:9], v0, off
.LBB0_912:
	s_or_b64 exec, exec, s[0:1]
	v_add_u32_e32 v8, s28, v59
	v_add_u32_e32 v0, v5, v19
	v_add_u32_e32 v5, v6, v23
	v_ashrrev_i32_e32 v9, 31, v8
	v_cmp_lt_i32_e32 vcc, v5, v17
	v_lshlrev_b64 v[8:9], 2, v[8:9]
	s_and_b64 s[0:1], s[58:59], vcc
	v_lshl_add_u64 v[8:9], s[26:27], 0, v[8:9]
	s_or_b64 s[2:3], s[56:57], s[0:1]
	global_store_dword v[8:9], v7, off
	s_and_saveexec_b64 s[0:1], s[2:3]
	s_cbranch_execz .LBB0_914
	v_min_i32_e32 v4, v5, v17
	v_add_u32_e32 v4, v4, v0
	v_add_u32_e32 v6, s33, v4
	v_ashrrev_i32_e32 v7, 31, v6
	v_lshlrev_b64 v[6:7], 2, v[6:7]
	v_lshl_add_u64 v[8:9], s[30:31], 0, v[6:7]
	v_lshl_add_u64 v[6:7], s[34:35], 0, v[6:7]
	global_store_dword v[6:7], v1, off
	v_add_u32_e32 v6, s44, v4
	v_ashrrev_i32_e32 v7, 31, v6
	v_lshl_add_u64 v[6:7], v[6:7], 2, s[36:37]
	global_store_dword v[8:9], v60, off
	global_store_dword v[6:7], v1, off
.LBB0_914:
	s_or_b64 exec, exec, s[0:1]
	v_add_u32_e32 v6, s28, v60
	v_ashrrev_i32_e32 v7, 31, v6
	v_lshlrev_b64 v[6:7], 2, v[6:7]
	v_cndmask_b32_e64 v8, 0, 1, s[58:59]
	v_lshl_add_u64 v[6:7], s[26:27], 0, v[6:7]
	global_store_dword v[6:7], v4, off
	v_add_u32_e32 v4, v5, v8
	v_cmp_lt_i32_e32 vcc, v4, v17
	v_cndmask_b32_e64 v1, 0, 1, s[56:57]
	s_and_b64 s[0:1], s[54:55], vcc
	v_add_u32_e32 v1, v0, v1
	s_or_b64 s[2:3], s[52:53], s[0:1]
	v_mov_b32_e32 v0, -1
	v_mov_b32_e32 v5, -1
	s_and_saveexec_b64 s[0:1], s[2:3]
	s_cbranch_execz .LBB0_916
	v_min_i32_e32 v5, v4, v17
	v_add_u32_e32 v5, v5, v1
	v_add_u32_e32 v6, s33, v5
	v_ashrrev_i32_e32 v7, 31, v6
	v_lshlrev_b64 v[6:7], 2, v[6:7]
	v_lshl_add_u64 v[8:9], s[30:31], 0, v[6:7]
	v_lshl_add_u64 v[6:7], s[34:35], 0, v[6:7]
	global_store_dword v[6:7], v2, off
	v_add_u32_e32 v6, s44, v5
	v_ashrrev_i32_e32 v7, 31, v6
	v_lshl_add_u64 v[6:7], v[6:7], 2, s[36:37]
	global_store_dword v[8:9], v61, off
	global_store_dword v[6:7], v2, off
.LBB0_916:
	s_or_b64 exec, exec, s[0:1]
	v_add_u32_e32 v6, s28, v61
	v_add_u32_e32 v2, v4, v18
	v_ashrrev_i32_e32 v7, 31, v6
	v_cmp_lt_i32_e32 vcc, v2, v17
	v_lshlrev_b64 v[6:7], 2, v[6:7]
	s_and_b64 s[0:1], s[50:51], vcc
	v_lshl_add_u64 v[6:7], s[26:27], 0, v[6:7]
	s_or_b64 s[2:3], s[48:49], s[0:1]
	global_store_dword v[6:7], v5, off
	s_and_saveexec_b64 s[0:1], s[2:3]
	s_cbranch_execz .LBB0_727
	v_min_i32_e32 v0, v2, v17
	v_add3_u32 v0, v1, v16, v0
	v_add_u32_e32 v4, s33, v0
	v_ashrrev_i32_e32 v5, 31, v4
	v_lshlrev_b64 v[4:5], 2, v[4:5]
	v_lshl_add_u64 v[6:7], s[30:31], 0, v[4:5]
	v_lshl_add_u64 v[4:5], s[34:35], 0, v[4:5]
	global_store_dword v[4:5], v3, off
	v_add_u32_e32 v4, s44, v0
	v_ashrrev_i32_e32 v5, 31, v4
	v_lshl_add_u64 v[4:5], v[4:5], 2, s[36:37]
	global_store_dword v[6:7], v62, off
	global_store_dword v[4:5], v3, off
	s_branch .LBB0_727

.LBB0_1241:
	s_or_b64 exec, exec, s[0:1]
	s_waitcnt lgkmcnt(0)
	s_barrier
	v_readlane_b32 s0, v235, 18
	v_ashrrev_i32_e32 v0, 5, v186
	v_and_b32_e32 v0, -2, v0
	v_add_u32_e32 v16, s0, v0
	s_movk_i32 s0, 0x4000
	v_cmp_gt_i32_e32 vcc, s0, v16
	s_and_saveexec_b64 s[0:1], vcc
	s_cbranch_execz .LBB0_1250
	s_load_dwordx2 s[4:5], s[46:47], 0x98
	s_load_dwordx4 s[0:3], s[46:47], 0x88
	v_and_b32_e32 v0, 15, v186
	v_mov_b32_e32 v19, 0
	v_lshlrev_b32_e32 v18, 15, v0
	v_bfe_u32 v0, v186, 4, 1
	v_lshl_or_b32 v18, v0, 2, v18
	s_waitcnt lgkmcnt(0)
	v_lshl_add_u64 v[0:1], s[4:5], 0, v[18:19]
	s_mov_b64 s[6:7], 0x15b000
	v_lshl_add_u64 v[20:21], v[0:1], 0, s[6:7]
	v_lshlrev_b32_e32 v0, 3, v186
	v_and_b32_e32 v0, 0x1f8, v0
	v_lshlrev_b32_e32 v18, 1, v0
	v_lshl_add_u64 v[2:3], s[4:5], 0, v[18:19]
	s_mov_b64 s[6:7], 0x9f73000
	v_lshl_add_u64 v[22:23], v[2:3], 0, s[6:7]
	s_mov_b64 s[6:7], 0x1b73000
	v_mbcnt_hi_u32_b32 v1, -1, v187
	v_lshl_add_u64 v[24:25], v[2:3], 0, s[6:7]
	v_and_b32_e32 v2, 64, v1
	v_add_u32_e32 v2, 64, v2
	v_xor_b32_e32 v3, 32, v1
	v_cmp_lt_i32_e32 vcc, v3, v2
	v_lshlrev_b32_e32 v18, 2, v0
	v_lshl_add_u64 v[26:27], s[0:1], 0, v[18:19]
	v_cndmask_b32_e32 v3, v1, v3, vcc
	v_lshlrev_b32_e32 v66, 2, v3
	v_xor_b32_e32 v3, 16, v1
	v_cmp_lt_i32_e32 vcc, v3, v2
	v_lshl_add_u64 v[28:29], s[2:3], 0, v[18:19]
	s_mov_b64 s[0:1], 0
	v_cndmask_b32_e32 v3, v1, v3, vcc
	v_lshlrev_b32_e32 v67, 2, v3
	v_xor_b32_e32 v3, 8, v1
	v_cmp_lt_i32_e32 vcc, v3, v2
	v_lshlrev_b32_e32 v18, 2, v0
	s_mov_b64 s[2:3], 0x5000
	v_cndmask_b32_e32 v3, v1, v3, vcc
	v_lshlrev_b32_e32 v68, 2, v3
	v_xor_b32_e32 v3, 4, v1
	v_cmp_lt_i32_e32 vcc, v3, v2
	s_movk_i32 s6, 0x5000
	v_mov_b32_e32 v72, 0x358637bd
	v_cndmask_b32_e32 v3, v1, v3, vcc
	v_lshlrev_b32_e32 v69, 2, v3
	v_xor_b32_e32 v3, 2, v1
	v_cmp_lt_i32_e32 vcc, v3, v2
	s_mov_b32 s7, 0x800000
	s_movk_i32 s8, 0x3fff
	v_cndmask_b32_e32 v3, v1, v3, vcc
	v_lshlrev_b32_e32 v70, 2, v3
	v_xor_b32_e32 v3, 1, v1
	v_cmp_lt_i32_e32 vcc, v3, v2
	s_nop 1
	v_cndmask_b32_e32 v1, v1, v3, vcc
	v_lshlrev_b32_e32 v71, 2, v1
	s_branch .LBB0_1244

.LBB0_1244:
	v_ashrrev_i32_e32 v17, 31, v16
	v_and_b32_e32 v0, 0x1fff, v16
	v_lshlrev_b32_e32 v0, 2, v0
	v_lshrrev_b32_e32 v1, 13, v16
	v_lshl_or_b32 v0, v1, 19, v0
	v_mov_b32_e32 v1, 0
	v_or_b32_e32 v30, 1, v16
	v_lshl_add_u64 v[0:1], v[20:21], 0, v[0:1]
	v_lshlrev_b64 v[2:3], 11, v[16:17]
	v_ashrrev_i32_e32 v31, 31, v30
	v_lshl_add_u64 v[32:33], v[22:23], 0, v[2:3]
	global_load_dword v65, v[0:1], off
	global_load_dwordx4 v[8:11], v[32:33], off
	v_lshlrev_b64 v[0:1], 11, v[30:31]
	v_lshl_add_u64 v[34:35], v[22:23], 0, v[0:1]
	global_load_dwordx4 v[12:15], v[32:33], off offset:1024
	global_load_dwordx4 v[4:7], v[34:35], off
	global_load_dwordx4 v[0:3], v[34:35], off offset:1024
	v_ashrrev_i32_e32 v64, 13, v16
	v_mov_b32_e32 v47, 0
	v_mov_b32_e32 v46, 0
	v_mov_b32_e32 v45, 0
	v_mov_b32_e32 v44, 0
	v_mov_b32_e32 v43, 0
	v_mov_b32_e32 v42, 0
	v_mov_b32_e32 v41, 0
	v_mov_b32_e32 v40, 0
	v_mov_b32_e32 v39, 0
	v_mov_b32_e32 v38, 0
	v_mov_b32_e32 v37, 0
	v_mov_b32_e32 v36, 0
	v_mov_b32_e32 v33, 0
	v_mov_b32_e32 v32, 0
	v_lshlrev_b32_e32 v73, 10, v64
	v_mov_b32_e32 v35, 0
	v_mov_b32_e32 v34, 0
	s_waitcnt vmcnt(4)
	v_cmp_lt_i32_e32 vcc, -1, v65
	s_and_b32 s9, vcc_lo, 0xffff
	s_cmp_eq_u32 s9, 0
	s_cbranch_scc1 .LBB0_1247
	v_mov_b32_e32 v34, 0
	v_mov_b32_e32 v35, v34
	v_mov_b32_e32 v32, v34
	v_mov_b32_e32 v33, v34
	v_mov_b32_e32 v36, v34
	v_mov_b32_e32 v37, v34
	v_mov_b32_e32 v38, v34
	v_mov_b32_e32 v39, v34
	v_mov_b32_e32 v40, v34
	v_mov_b32_e32 v41, v34
	v_mov_b32_e32 v42, v34
	v_mov_b32_e32 v43, v34
	v_mov_b32_e32 v44, v34
	v_mov_b32_e32 v45, v34
	v_mov_b32_e32 v46, v34
	v_mov_b32_e32 v47, v34
